# speedup vs baseline: 1.0018x; 1.0018x over previous
_Z8k_expertPKDF16_S0_PKfPcPiS0_S2_S2_S2_S2_PfS5_S4_S2_S2_S2_S2_S5_S2_S2_S2_:
	s_lshl_b32 s3, s2, 2
	s_load_dwordx8 s[8:15], s[0:1], 0x88
	s_load_dwordx2 s[70:71], s[0:1], 0x0
	s_and_b32 s3, s3, 28
	s_ashr_i32 s4, s2, 6
	s_add_i32 s34, s3, s4
	s_ashr_i32 s6, s34, 1
	v_mov_b32_e32 v2, v0
	s_lshl_b32 s4, s6, 4
	s_ashr_i32 s5, s4, 31
	v_ashrrev_i32_e32 v3, 31, v2
	s_waitcnt lgkmcnt(0)
	s_load_dwordx8 s[16:23], s[14:15], 0x0
	v_lshl_add_u64 v[4:5], v[2:3], 2, s[10:11]
	s_lshl_b64 s[10:11], s[4:5], 11
	v_lshl_add_u64 v[6:7], v[4:5], 0, s[10:11]
	s_or_b32 s10, s4, 1
	s_ashr_i32 s11, s10, 31
	s_lshl_b64 s[10:11], s[10:11], 11
	v_lshl_add_u64 v[8:9], v[4:5], 0, s[10:11]
	s_or_b32 s10, s4, 2
	s_ashr_i32 s11, s10, 31
	s_lshl_b64 s[10:11], s[10:11], 11
	v_lshl_add_u64 v[10:11], v[4:5], 0, s[10:11]
	s_or_b32 s10, s4, 3
	s_ashr_i32 s11, s10, 31
	s_lshl_b64 s[10:11], s[10:11], 11
	v_lshl_add_u64 v[12:13], v[4:5], 0, s[10:11]
	s_or_b32 s10, s4, 4
	s_ashr_i32 s11, s10, 31
	s_lshl_b64 s[10:11], s[10:11], 11
	v_lshl_add_u64 v[14:15], v[4:5], 0, s[10:11]
	s_or_b32 s10, s4, 5
	s_ashr_i32 s11, s10, 31
	s_lshl_b64 s[10:11], s[10:11], 11
	v_lshl_add_u64 v[16:17], v[4:5], 0, s[10:11]
	s_or_b32 s10, s4, 6
	s_ashr_i32 s11, s10, 31
	s_lshl_b64 s[10:11], s[10:11], 11
	v_lshl_add_u64 v[18:19], v[4:5], 0, s[10:11]
	s_or_b32 s10, s4, 7
	s_ashr_i32 s11, s10, 31
	s_lshl_b64 s[10:11], s[10:11], 11
	v_lshl_add_u64 v[20:21], v[4:5], 0, s[10:11]
	s_or_b32 s10, s4, 8
	s_ashr_i32 s11, s10, 31
	s_lshl_b64 s[10:11], s[10:11], 11
	global_load_dword v1, v[6:7], off
	global_load_dword v3, v[8:9], off
	global_load_dword v22, v[10:11], off
	global_load_dword v23, v[12:13], off
	global_load_dword v24, v[14:15], off
	global_load_dword v25, v[16:17], off
	global_load_dword v26, v[18:19], off
	global_load_dword v27, v[20:21], off
	v_lshl_add_u64 v[6:7], v[4:5], 0, s[10:11]
	s_or_b32 s10, s4, 9
	s_ashr_i32 s11, s10, 31
	s_lshl_b64 s[10:11], s[10:11], 11
	v_lshl_add_u64 v[8:9], v[4:5], 0, s[10:11]
	s_or_b32 s10, s4, 10
	s_ashr_i32 s11, s10, 31
	s_lshl_b64 s[10:11], s[10:11], 11
	v_lshl_add_u64 v[10:11], v[4:5], 0, s[10:11]
	s_or_b32 s10, s4, 11
	s_ashr_i32 s11, s10, 31
	s_lshl_b64 s[10:11], s[10:11], 11
	v_lshl_add_u64 v[12:13], v[4:5], 0, s[10:11]
	s_or_b32 s10, s4, 12
	s_ashr_i32 s11, s10, 31
	s_lshl_b64 s[10:11], s[10:11], 11
	v_lshl_add_u64 v[14:15], v[4:5], 0, s[10:11]
	s_or_b32 s10, s4, 13
	s_ashr_i32 s11, s10, 31
	s_lshl_b64 s[10:11], s[10:11], 11
	v_lshl_add_u64 v[16:17], v[4:5], 0, s[10:11]
	s_or_b32 s10, s4, 14
	s_or_b32 s4, s4, 15
	s_ashr_i32 s11, s10, 31
	s_ashr_i32 s5, s4, 31
	s_lshl_b64 s[10:11], s[10:11], 11
	s_lshl_b64 s[4:5], s[4:5], 11
	v_lshl_add_u64 v[18:19], v[4:5], 0, s[10:11]
	v_lshl_add_u64 v[4:5], v[4:5], 0, s[4:5]
	global_load_dword v20, v[6:7], off
	global_load_dword v21, v[8:9], off
	global_load_dword v28, v[10:11], off
	global_load_dword v29, v[12:13], off
	global_load_dword v30, v[14:15], off
	global_load_dword v31, v[16:17], off
	global_load_dword v32, v[18:19], off
	global_load_dword v33, v[4:5], off
	v_lshlrev_b32_e32 v4, 3, v2
	v_ashrrev_i32_e32 v5, 31, v4
	v_lshl_add_u64 v[12:13], v[4:5], 2, s[12:13]
	global_load_dwordx4 v[4:7], v[12:13], off
	global_load_dwordx4 v[8:11], v[12:13], off offset:16
	s_waitcnt vmcnt(17)
	v_add_f32_e32 v1, 0, v1
	s_waitcnt vmcnt(16)
	v_add_f32_e32 v1, v1, v3
	s_waitcnt vmcnt(15)
	v_add_f32_e32 v1, v1, v22
	s_waitcnt vmcnt(14)
	v_add_f32_e32 v1, v1, v23
	s_waitcnt vmcnt(13)
	v_add_f32_e32 v1, v1, v24
	s_waitcnt vmcnt(12)
	v_add_f32_e32 v1, v1, v25
	s_waitcnt vmcnt(11)
	v_add_f32_e32 v1, v1, v26
	s_waitcnt vmcnt(10)
	v_add_f32_e32 v1, v1, v27
	s_waitcnt vmcnt(9)
	v_add_f32_e32 v1, v1, v20
	s_waitcnt vmcnt(8)
	v_add_f32_e32 v1, v1, v21
	s_waitcnt vmcnt(7)
	v_add_f32_e32 v1, v1, v28
	s_waitcnt vmcnt(6)
	v_add_f32_e32 v1, v1, v29
	s_waitcnt vmcnt(5)
	v_add_f32_e32 v1, v1, v30
	s_waitcnt vmcnt(4)
	v_add_f32_e32 v1, v1, v31
	s_waitcnt vmcnt(3)
	v_add_f32_e32 v1, v1, v32
	s_waitcnt vmcnt(2)
	v_add_f32_e32 v1, v1, v33
	v_mul_f32_e32 v12, 0x3a800000, v1
	v_and_b32_e32 v200, 63, v0
	v_lshrrev_b32_e32 v201, 6, v0
	v_lshlrev_b32_e32 v202, 4, v200
	v_and_b32_e32 v203, 32, v200
	v_xor_b32_e32 v202, v202, v203
	v_lshrrev_b32_e32 v203, 6, v202
	v_lshrrev_b32_e32 v204, 1, v201
	v_lshl_add_u32 v203, v204, 4, v203
	v_and_b32_e32 v204, 62, v202
	v_and_b32_e32 v205, 1, v201
	v_lshl_add_u32 v204, v205, 6, v204
	v_lshl_add_u32 v200, v203, 12, v204
	v_add_u32_e32 v201, 0x40000, v200
	s_lshl_b32 s72, s6, 22
	s_lshr_b32 s73, s2, 4
	s_and_b32 s73, s73, 3
	s_lshl_b32 s73, s73, 20
	s_add_u32 s72, s72, s73
	s_add_u32 s74, s70, s72
	s_addc_u32 s75, s71, 0
	s_add_u32 s76, s74, 0x80000
	s_addc_u32 s77, s75, 0
	v_readfirstlane_b32 s78, v0
	s_lshl_b32 s78, s78, 4
	s_mov_b32 m0, s78
	s_add_i32 s79, s78, 0x2000
	global_load_lds_dwordx4 v200, s[74:75]
	s_mov_b32 m0, s79
	s_add_i32 s79, s78, 0x4000
	global_load_lds_dwordx4 v201, s[74:75]
	s_mov_b32 m0, s79
	s_add_i32 s79, s78, 0x6000
	global_load_lds_dwordx4 v200, s[76:77]
	s_mov_b32 m0, s79
	s_nop 0
	global_load_lds_dwordx4 v201, s[76:77]
	v_mbcnt_lo_u32_b32 v1, -1, 0
	v_mbcnt_hi_u32_b32 v3, -1, v1
	v_xor_b32_e32 v13, 32, v3
	v_lshlrev_b32_e32 v183, 2, v13
	v_xor_b32_e32 v13, 16, v3
	v_lshlrev_b32_e32 v181, 2, v13
	v_xor_b32_e32 v13, 8, v3
	v_lshlrev_b32_e32 v1, 2, v13
	v_xor_b32_e32 v13, 4, v3
	v_lshlrev_b32_e32 v180, 2, v13
	v_xor_b32_e32 v13, 2, v3
	v_lshlrev_b32_e32 v182, 2, v13
	v_xor_b32_e32 v13, 1, v3
	v_lshlrev_b32_e32 v184, 2, v13
	v_cmp_eq_u32_e32 vcc, 0, v3
	v_mov_b32_e32 v13, v12
	s_waitcnt vmcnt(4)
	v_pk_mul_f32 v[14:15], v[12:13], v[4:5]
	v_pk_mul_f32 v[16:17], v[12:13], v[6:7]
	v_pk_mul_f32 v[18:19], v[12:13], v[8:9]
	v_pk_mul_f32 v[20:21], v[12:13], v[10:11]
	v_add_f32_dpp v14, v14, v14 quad_perm:[1,0,3,2] row_mask:0xf bank_mask:0xf
	v_add_f32_dpp v15, v15, v15 quad_perm:[1,0,3,2] row_mask:0xf bank_mask:0xf
	v_add_f32_dpp v16, v16, v16 quad_perm:[1,0,3,2] row_mask:0xf bank_mask:0xf
	v_add_f32_dpp v17, v17, v17 quad_perm:[1,0,3,2] row_mask:0xf bank_mask:0xf
	v_add_f32_dpp v18, v18, v18 quad_perm:[1,0,3,2] row_mask:0xf bank_mask:0xf
	v_add_f32_dpp v19, v19, v19 quad_perm:[1,0,3,2] row_mask:0xf bank_mask:0xf
	v_add_f32_dpp v20, v20, v20 quad_perm:[1,0,3,2] row_mask:0xf bank_mask:0xf
	v_add_f32_dpp v21, v21, v21 quad_perm:[1,0,3,2] row_mask:0xf bank_mask:0xf
	v_add_f32_dpp v14, v14, v14 quad_perm:[2,3,0,1] row_mask:0xf bank_mask:0xf
	v_add_f32_dpp v15, v15, v15 quad_perm:[2,3,0,1] row_mask:0xf bank_mask:0xf
	v_add_f32_dpp v16, v16, v16 quad_perm:[2,3,0,1] row_mask:0xf bank_mask:0xf
	v_add_f32_dpp v17, v17, v17 quad_perm:[2,3,0,1] row_mask:0xf bank_mask:0xf
	v_add_f32_dpp v18, v18, v18 quad_perm:[2,3,0,1] row_mask:0xf bank_mask:0xf
	v_add_f32_dpp v19, v19, v19 quad_perm:[2,3,0,1] row_mask:0xf bank_mask:0xf
	v_add_f32_dpp v20, v20, v20 quad_perm:[2,3,0,1] row_mask:0xf bank_mask:0xf
	v_add_f32_dpp v21, v21, v21 quad_perm:[2,3,0,1] row_mask:0xf bank_mask:0xf
	v_add_f32_dpp v14, v14, v14 row_half_mirror row_mask:0xf bank_mask:0xf
	v_add_f32_dpp v15, v15, v15 row_half_mirror row_mask:0xf bank_mask:0xf
	v_add_f32_dpp v16, v16, v16 row_half_mirror row_mask:0xf bank_mask:0xf
	v_add_f32_dpp v17, v17, v17 row_half_mirror row_mask:0xf bank_mask:0xf
	v_add_f32_dpp v18, v18, v18 row_half_mirror row_mask:0xf bank_mask:0xf
	v_add_f32_dpp v19, v19, v19 row_half_mirror row_mask:0xf bank_mask:0xf
	v_add_f32_dpp v20, v20, v20 row_half_mirror row_mask:0xf bank_mask:0xf
	v_add_f32_dpp v21, v21, v21 row_half_mirror row_mask:0xf bank_mask:0xf
	v_add_f32_dpp v14, v14, v14 row_mirror row_mask:0xf bank_mask:0xf
	v_add_f32_dpp v15, v15, v15 row_mirror row_mask:0xf bank_mask:0xf
	v_add_f32_dpp v16, v16, v16 row_mirror row_mask:0xf bank_mask:0xf
	v_add_f32_dpp v17, v17, v17 row_mirror row_mask:0xf bank_mask:0xf
	v_add_f32_dpp v18, v18, v18 row_mirror row_mask:0xf bank_mask:0xf
	v_add_f32_dpp v19, v19, v19 row_mirror row_mask:0xf bank_mask:0xf
	v_add_f32_dpp v20, v20, v20 row_mirror row_mask:0xf bank_mask:0xf
	v_add_f32_dpp v21, v21, v21 row_mirror row_mask:0xf bank_mask:0xf
	ds_bpermute_b32 v22, v181, v14
	ds_bpermute_b32 v23, v181, v15
	ds_bpermute_b32 v24, v181, v16
	ds_bpermute_b32 v25, v181, v17
	ds_bpermute_b32 v26, v181, v18
	ds_bpermute_b32 v27, v181, v19
	ds_bpermute_b32 v28, v181, v20
	ds_bpermute_b32 v29, v181, v21
	s_waitcnt lgkmcnt(0)
	v_pk_add_f32 v[14:15], v[14:15], v[22:23]
	v_pk_add_f32 v[16:17], v[16:17], v[24:25]
	v_pk_add_f32 v[18:19], v[18:19], v[26:27]
	v_pk_add_f32 v[20:21], v[20:21], v[28:29]
	ds_bpermute_b32 v22, v183, v14
	ds_bpermute_b32 v23, v183, v15
	ds_bpermute_b32 v24, v183, v16
	ds_bpermute_b32 v25, v183, v17
	ds_bpermute_b32 v26, v183, v18
	ds_bpermute_b32 v27, v183, v19
	ds_bpermute_b32 v28, v183, v20
	ds_bpermute_b32 v29, v183, v21
	s_waitcnt lgkmcnt(0)
	v_pk_add_f32 v[14:15], v[14:15], v[22:23]
	v_pk_add_f32 v[16:17], v[16:17], v[24:25]
	v_pk_add_f32 v[18:19], v[18:19], v[26:27]
	v_pk_add_f32 v[20:21], v[20:21], v[28:29]
	s_and_saveexec_b64 s[4:5], vcc
	s_cbranch_execz .LBB5_2
	v_lshrrev_b32_e32 v22, 1, v0
	v_add_u32_e32 v22, 0x20000, v22
	ds_write_b128 v22, v[14:17]
	ds_write_b128 v22, v[18:21] offset:16
